# MoE bias tables (gate/up and down phases) filled by direct HBM->LDS loads with one wait, instead of gather -> wait -> ds_write per iteration; on top of v6
# speedup vs baseline: 1.0074x; 1.0010x over previous
.LBB0_1313:
	s_or_b64 exec, exec, s[0:1]
	s_mov_b64 s[4:5], s[86:87]
	s_waitcnt lgkmcnt(0)
	s_barrier
	s_and_saveexec_b64 s[0:1], vcc
	s_cbranch_execz .LBB0_1322
	s_lshl_b32 s66, s92, 2
	s_add_i32 s66, s66, 0x22a00
	s_load_dwordx2 s[10:11], s[4:5], 0xf8
	s_load_dwordx2 s[12:13], s[4:5], 0x108
	s_movk_i32 s4, 0x7f
	v_lshl_add_u32 v1, v8, 2, 0
	s_movk_i32 s16, 0xfe00
	v_cmp_lt_u32_e32 vcc, s4, v0
	v_add_u32_e32 v13, 0x22a00, v1
	s_mov_b64 s[14:15], 0
	v_mov_b32_e32 v1, 0
	s_mov_b32 s17, -1
	s_movk_i32 s20, 0xfff
	v_lshlrev_b32_e32 v0, 2, v0
	v_mov_b32_e32 v14, v8
	s_branch .LBB0_1317
.LBB0_1315:
	s_mov_b32 m0, s66
	s_or_b64 exec, exec, s[4:5]
	s_nop 0
	global_load_lds_dword v[4:5], off
.LBB0_1316:
	s_or_b64 exec, exec, s[18:19]
	s_add_i32 s66, s66, 0x800
	v_add_u32_e32 v2, 0x200, v14
	v_cmp_lt_i32_e64 s[4:5], s20, v14
	v_add_u32_e32 v13, 0x800, v13
	s_or_b64 s[14:15], s[4:5], s[14:15]
	v_mov_b32_e32 v14, v2
	s_andn2_b64 exec, exec, s[14:15]
	s_cbranch_execz .LBB0_1322

.LBB0_1322:
	s_or_b64 exec, exec, s[0:1]
	s_mov_b64 s[0:1], s[86:87]
	s_waitcnt vmcnt(0) lgkmcnt(0)
	s_barrier
	s_add_i32 s0, 0, 0x20200
	v_mov_b32_e32 v0, s0
	ds_read_b32 v0, v0
	v_readfirstlane_b32 s24, v8
	s_waitcnt lgkmcnt(0)
	v_readfirstlane_b32 s50, v0
	s_cmp_lt_i32 s50, 0
	s_cbranch_scc1 .LBB0_1341
	v_ashrrev_i32_e32 v1, 31, v10
	v_lshrrev_b32_e32 v1, 22, v1
	v_add_u32_e32 v1, v10, v1
	v_and_b32_e32 v1, 0xfffffc00, v1
	v_sub_u32_e32 v1, v10, v1
	v_lshrrev_b32_e32 v2, 4, v1
	v_bitop3_b32 v2, v2, v1, 32 bitop3:0x6c
	v_ashrrev_i32_e32 v1, 31, v1
	v_ashrrev_i32_e32 v0, 31, v8
	v_lshrrev_b32_e32 v1, 26, v1
	v_lshrrev_b32_e32 v0, 26, v0
	v_add_u32_e32 v1, v2, v1
	v_add_u32_e32 v0, v8, v0
	v_ashrrev_i32_e32 v4, 6, v1
	v_and_b32_e32 v1, 0xc0, v1
	v_ashrrev_i32_e32 v0, 6, v0
	v_sub_u32_e32 v1, v2, v1
	v_mov_b32_e32 v2, 1
	v_lshlrev_b32_e32 v3, 3, v0
	v_lshlrev_b32_e32 v0, 5, v0
	v_ashrrev_i16_sdwa v1, v2, sext(v1) dst_sel:DWORD dst_unused:UNUSED_PAD src0_sel:DWORD src1_sel:BYTE_0
	v_and_b32_e32 v0, 32, v0
	v_bfe_i32 v1, v1, 0, 16
	v_add_lshl_u32 v181, v0, v1, 1
	v_sub_u32_e32 v0, v9, v12
	v_lshrrev_b32_e32 v1, 4, v0
	v_bitop3_b32 v1, v1, v0, 32 bitop3:0x6c
	v_ashrrev_i32_e32 v0, 31, v0
	v_lshrrev_b32_e32 v0, 26, v0
	v_and_b32_e32 v3, -16, v3
	v_add_u32_e32 v0, v1, v0
	v_add_u32_e32 v180, v4, v3
	v_lshlrev_b32_e32 v3, 3, v11
	v_ashrrev_i32_e32 v5, 6, v0
	v_and_b32_e32 v0, 0xc0, v0
	v_and_b32_e32 v3, -16, v3
	v_sub_u32_e32 v0, v1, v0
	v_add_u32_e32 v182, v5, v3
	v_lshlrev_b32_e32 v3, 5, v11
	v_ashrrev_i16_sdwa v0, v2, sext(v0) dst_sel:DWORD dst_unused:UNUSED_PAD src0_sel:DWORD src1_sel:BYTE_0
	v_and_b32_e32 v3, 32, v3
	v_bfe_i32 v0, v0, 0, 16
	s_ashr_i32 s4, s24, 6
	v_add_lshl_u32 v183, v3, v0, 1
	v_and_b32_e32 v0, 3, v5
	s_mov_b32 s10, 0x1fffe0
	v_lshrrev_b32_e32 v1, 2, v182
	v_lshlrev_b32_e32 v2, 1, v182
	s_ashr_i32 s12, s24, 8
	s_lshl_b32 s5, s4, 10
	v_and_or_b32 v0, v182, s10, v0
	v_and_b32_e32 v1, 4, v1
	v_and_b32_e32 v3, 24, v2
	s_add_u32 s0, s8, 0x70700000
	v_or3_b32 v0, v0, v1, v3
	s_addc_u32 s1, s9, 0
	v_lshl_add_u32 v152, v0, 11, v183
	v_and_b32_e32 v0, 3, v4
	v_lshrrev_b32_e32 v1, 2, v180
	v_lshlrev_b32_e32 v3, 1, v180
	s_add_u32 s25, s8, 0x4e00000
	v_and_or_b32 v0, v180, s10, v0
	v_and_b32_e32 v1, 4, v1
	v_and_b32_e32 v4, 24, v3
	s_addc_u32 s26, s9, 0
	v_or3_b32 v0, v0, v1, v4
	s_add_i32 s10, 0, 0x20204
	v_lshl_add_u32 v154, v0, 11, v181
	v_mov_b32_e32 v0, s10
	ds_read2_b32 v[0:1], v0 offset1:1
	s_add_i32 s10, 0, 0x20600
	v_add_u32_e32 v2, s10, v2
	ds_read_u16 v4, v2 offset:256
	v_add_u32_e32 v3, s10, v3
	s_waitcnt lgkmcnt(1)
	v_readfirstlane_b32 s51, v0
	v_readfirstlane_b32 s10, v1
	s_lshl_b32 s14, s51, 8
	s_ashr_i32 s11, s10, 31
	s_ashr_i32 s15, s14, 31
	s_lshl_b64 s[10:11], s[10:11], 23
	s_lshl_b64 s[14:15], s[14:15], 11
	s_add_u32 s10, s25, s10
	s_addc_u32 s11, s26, s11
	s_add_u32 s16, s10, s14
	s_addc_u32 s17, s11, s15
	s_add_i32 s27, s5, 0
	ds_read_u16 v0, v3
	ds_read_u16 v1, v2
	ds_read_u16 v2, v3 offset:256
	s_add_i32 s28, s27, 0x10000
	s_mov_b32 m0, s28
	s_add_i32 s29, s27, 0x12000
	global_load_lds_dwordx4 v154, s[16:17]
	s_mov_b32 m0, s29
	s_add_i32 s30, s27, 0x2000
	s_waitcnt lgkmcnt(0)
	v_lshl_add_u32 v156, v0, 11, v181
	global_load_lds_dwordx4 v152, s[16:17]
	s_mov_b32 m0, s27
	s_add_u32 s10, s16, 0x40000
	v_lshl_add_u32 v166, v1, 11, v183
	global_load_lds_dwordx4 v156, s[0:1]
	s_mov_b32 m0, s30
	s_addc_u32 s11, s17, 0
	s_add_i32 s31, s27, 0x14000
	global_load_lds_dwordx4 v166, s[0:1]
	s_mov_b32 m0, s31
	s_add_i32 s33, s27, 0x16000
	global_load_lds_dwordx4 v154, s[10:11]
	s_mov_b32 m0, s33
	s_add_i32 s34, s27, 0x4000
	v_lshl_add_u32 v164, v2, 11, v181
	global_load_lds_dwordx4 v152, s[10:11]
	s_mov_b32 m0, s34
	s_add_i32 s35, s27, 0x6000
	v_lshl_add_u32 v162, v4, 11, v183
	global_load_lds_dwordx4 v164, s[0:1]
	s_mov_b32 m0, s35
	v_mov_b32_e32 v157, 0
	global_load_lds_dwordx4 v162, s[0:1]
	v_mov_b32_e32 v155, v157
	v_mov_b32_e32 v153, v157
	v_lshl_add_u64 v[2:3], s[16:17], 0, v[154:155]
	v_lshl_add_u64 v[0:1], s[16:17], 0, v[152:153]
	s_cmp_lg_u32 s12, 1
	v_mov_b32_e32 v167, v157
	s_cbranch_scc1 .LBB0_1325
	s_barrier

.LBB0_1404:
	s_or_b64 exec, exec, s[8:9]
	s_movk_i32 s4, 0x1200
	v_mul_i32_i24_e32 v2, 0x400, v9
	v_cmp_gt_i32_e32 vcc, s4, v8
	s_mov_b64 s[8:9], s[86:87]
	s_waitcnt lgkmcnt(0)
	s_barrier
	s_and_saveexec_b64 s[4:5], vcc
	s_cbranch_execz .LBB0_1409
	s_lshl_b32 s66, s92, 2
	s_add_i32 s66, s66, 0x22a00
	s_load_dwordx2 s[8:9], s[8:9], 0x118
	v_and_b32_e32 v0, 0xff, v8
	v_lshl_add_u32 v3, v8, 2, 0
	v_mov_b32_e32 v1, 0
	v_add_u32_e32 v3, 0x22a00, v3
	s_mov_b64 s[10:11], 0
	v_lshlrev_b32_e32 v0, 2, v0
	s_movk_i32 s14, 0xfff
	v_mov_b32_e32 v6, v8
	s_branch .LBB0_1407
.LBB0_1406:
	s_or_b64 exec, exec, s[12:13]
	s_add_i32 s66, s66, 0x800
	v_add_u32_e32 v7, 0x200, v6
	v_cmp_lt_i32_e32 vcc, s14, v6
	v_add_u32_e32 v3, 0x800, v3
	s_or_b64 s[10:11], vcc, s[10:11]
	v_mov_b32_e32 v6, v7
	s_andn2_b64 exec, exec, s[10:11]
	s_cbranch_execz .LBB0_1409
.LBB0_1407:
	v_ashrrev_i32_e32 v7, 6, v6
	v_lshlrev_b32_e32 v7, 2, v7
	v_and_b32_e32 v7, -16, v7
	v_add_u32_e32 v7, 0, v7
	v_add_u32_e32 v7, 0x20200, v7
	ds_read_b32 v10, v7
	s_waitcnt lgkmcnt(0)
	v_cmp_lt_i32_e32 vcc, -1, v10
	s_and_saveexec_b64 s[12:13], vcc
	s_cbranch_execz .LBB0_1406
	ds_read2_b32 v[10:11], v7 offset0:1 offset1:2
	s_waitcnt lgkmcnt(0)
	v_ashrrev_i32_e32 v13, 31, v11
	v_mov_b32_e32 v12, v11
	v_lshlrev_b32_e32 v10, 8, v10
	v_lshlrev_b64 v[12:13], 13, v[12:13]
	v_ashrrev_i32_e32 v11, 31, v10
	v_lshl_add_u64 v[12:13], s[8:9], 0, v[12:13]
	v_lshl_add_u64 v[10:11], v[10:11], 2, v[12:13]
	v_lshl_add_u64 v[10:11], v[10:11], 0, v[0:1]
	s_mov_b32 m0, s66
	s_nop 0
	global_load_lds_dword v[10:11], off
	s_branch .LBB0_1406
.LBB0_1409:
	s_or_b64 exec, exec, s[4:5]
	s_mov_b64 s[4:5], s[86:87]
	s_waitcnt vmcnt(0) lgkmcnt(0)
	s_barrier
	s_add_i32 s4, 0, 0x20200
	v_mov_b32_e32 v0, s4
	ds_read_b32 v0, v0
	v_readfirstlane_b32 s24, v8
	s_mov_b32 s17, 0
	s_waitcnt lgkmcnt(0)
	v_readfirstlane_b32 s16, v0
	s_cmp_lt_i32 s16, 0
	s_cbranch_scc1 .LBB0_1424
	v_sub_u32_e32 v0, v5, v2
	v_lshrrev_b32_e32 v1, 4, v0
	v_bitop3_b32 v1, v1, v0, 32 bitop3:0x6c
	v_ashrrev_i32_e32 v0, 31, v0
	v_lshrrev_b32_e32 v0, 26, v0
	v_add_u32_e32 v0, v1, v0
	v_ashrrev_i32_e32 v10, 6, v0
	v_lshlrev_b32_e32 v2, 3, v9
	v_and_b32_e32 v0, 0xc0, v0
	v_and_b32_e32 v2, -16, v2
	v_sub_u32_e32 v0, v1, v0
	v_mov_b32_e32 v1, 1
	v_add_u32_e32 v2, v10, v2
	v_ashrrev_i16_sdwa v0, v1, sext(v0) dst_sel:DWORD dst_unused:UNUSED_PAD src0_sel:DWORD src1_sel:BYTE_0
	v_and_b32_e32 v3, 3, v10
	s_mov_b32 s9, 0x1fffe0
	v_lshrrev_b32_e32 v5, 2, v2
	v_lshlrev_b32_e32 v6, 1, v2
	v_bfe_i32 v11, v0, 0, 16
	v_ashrrev_i32_e32 v0, 31, v4
	v_and_or_b32 v3, v2, s9, v3
	v_and_b32_e32 v5, 4, v5
	v_and_b32_e32 v6, 24, v6
	v_lshrrev_b32_e32 v0, 22, v0
	v_or3_b32 v3, v3, v5, v6
	v_lshlrev_b32_e32 v5, 5, v9
	v_add_u32_e32 v0, v4, v0
	v_and_b32_e32 v5, 32, v5
	v_and_b32_e32 v0, 0xfffffc00, v0
	v_add_lshl_u32 v5, v5, v11, 1
	v_sub_u32_e32 v0, v4, v0
	v_ashrrev_i32_e32 v4, 31, v8
	v_lshl_add_u32 v144, v3, 11, v5
	v_lshrrev_b32_e32 v3, 4, v0
	v_lshrrev_b32_e32 v4, 26, v4
	v_bitop3_b32 v3, v3, v0, 32 bitop3:0x6c
	v_ashrrev_i32_e32 v0, 31, v0
	v_add_u32_e32 v4, v8, v4
	s_ashr_i32 s4, s24, 6
	v_lshrrev_b32_e32 v0, 26, v0
	v_ashrrev_i32_e32 v13, 6, v4
	s_ashr_i32 s8, s24, 8
	s_lshl_b32 s5, s4, 10
	v_add_u32_e32 v0, v3, v0
	v_lshlrev_b32_e32 v4, 3, v13
	s_add_u32 s25, s6, 0x34e00000
	v_ashrrev_i32_e32 v12, 6, v0
	v_and_b32_e32 v4, -16, v4
	s_addc_u32 s26, s7, 0
	v_add_u32_e32 v4, v12, v4
	v_and_b32_e32 v0, 0xc0, v0
	s_add_u32 s27, s6, 0x24e00000
	v_and_b32_e32 v6, 3, v12
	v_lshrrev_b32_e32 v7, 2, v4
	v_lshlrev_b32_e32 v14, 1, v4
	v_sub_u32_e32 v0, v3, v0
	s_addc_u32 s28, s7, 0
	v_and_or_b32 v6, v4, s9, v6
	v_and_b32_e32 v7, 4, v7
	v_and_b32_e32 v14, 24, v14
	v_ashrrev_i16_sdwa v0, v1, sext(v0) dst_sel:DWORD dst_unused:UNUSED_PAD src0_sel:DWORD src1_sel:BYTE_0
	s_add_i32 s9, 0, 0x20204
	v_or3_b32 v6, v6, v7, v14
	v_bfe_i32 v14, v0, 0, 16
	v_mov_b32_e32 v0, s9
	ds_read2_b32 v[0:1], v0 offset1:1
	s_lshl_b64 s[10:11], s[16:17], 19
	s_add_u32 s18, s25, s10
	s_addc_u32 s19, s26, s11
	v_lshlrev_b32_e32 v7, 5, v13
	s_waitcnt lgkmcnt(0)
	v_readfirstlane_b32 s54, v0
	v_readfirstlane_b32 s10, v1
	s_lshl_b32 s12, s54, 8
	s_ashr_i32 s11, s10, 31
	s_ashr_i32 s13, s12, 31
	s_lshl_b64 s[10:11], s[10:11], 22
	s_lshl_b64 s[12:13], s[12:13], 11
	s_add_u32 s9, s27, s10
	s_addc_u32 s10, s28, s11
	s_add_u32 s20, s9, s12
	v_and_b32_e32 v7, 32, v7
	s_addc_u32 s21, s10, s13
	s_add_i32 s29, s5, 0
	v_add_lshl_u32 v3, v7, v14, 1
	s_add_i32 s30, s29, 0x10000
	v_lshl_add_u32 v146, v6, 11, v3
	s_mov_b32 m0, s30
	s_add_i32 s31, s29, 0x12000
	global_load_lds_dwordx4 v146, s[20:21]
	s_mov_b32 m0, s31
	s_add_i32 s33, s29, 0x2000
	v_lshl_add_u32 v148, v4, 11, v3
	global_load_lds_dwordx4 v144, s[20:21]
	s_mov_b32 m0, s29
	s_add_u32 s10, s20, 0x40000
	v_lshl_add_u32 v150, v2, 11, v5
	global_load_lds_dwordx4 v148, s[18:19]
	s_mov_b32 m0, s33
	s_addc_u32 s11, s21, 0
	s_add_i32 s34, s29, 0x14000
	global_load_lds_dwordx4 v150, s[18:19]
	s_mov_b32 m0, s34
	s_add_i32 s35, s29, 0x16000
	global_load_lds_dwordx4 v146, s[10:11]
	s_mov_b32 m0, s35
	s_add_i32 s36, s29, 0x4000
	v_add_u32_e32 v152, 0x40000, v148
	global_load_lds_dwordx4 v144, s[10:11]
	s_mov_b32 m0, s36
	s_add_i32 s37, s29, 0x6000
	v_add_u32_e32 v154, 0x40000, v150
	global_load_lds_dwordx4 v152, s[18:19]
	s_mov_b32 m0, s37
	v_mov_b32_e32 v147, 0
	global_load_lds_dwordx4 v154, s[18:19]
	v_mov_b32_e32 v145, v147
	v_mov_b32_e32 v149, v147
	v_mov_b32_e32 v151, v147
	s_mov_b32 s38, 0x40000
	v_lshl_add_u64 v[6:7], s[20:21], 0, v[146:147]
	s_mov_b32 s39, 0x10000
	v_lshl_add_u64 v[4:5], s[20:21], 0, v[144:145]
	v_lshl_add_u64 v[2:3], s[18:19], 0, v[148:149]
	s_cmp_lg_u32 s8, 1
	v_lshl_add_u64 v[0:1], s[18:19], 0, v[150:151]
	s_cbranch_scc1 .LBB0_1412
	s_barrier
